# P7: next-step row prefetch issued after the router MFMA loop, b_router load hoisted out of top-k loop, norm-loop leading waits lowered for the younger top-k stores
# speedup vs baseline: 1.0185x; 1.0004x over previous
.LBB0_1137:
	s_add_i32 s16, s63, s62
	s_lshl_b32 s17, s16, 12
	s_or_b32 s22, s16, 1
	s_and_b32 s17, s17, 0x3e000
	s_add_u32 s18, s33, s17
	s_addc_u32 s19, s53, 0
	s_ashr_i32 s20, s16, 6
	v_mov_b32_e32 v209, v206
	s_ashr_i32 s21, s20, 31
	s_lshl_b64 s[20:21], s[20:21], 12
	v_lshlrev_b32_e32 v142, 2, v209
	s_add_u32 s20, s33, s20
	v_ashrrev_i32_e32 v143, 31, v142
	s_addc_u32 s21, s53, s21
	v_lshlrev_b64 v[170:171], 2, v[142:143]
	v_lshl_add_u64 v[70:71], s[20:21], 0, v[170:171]
	s_waitcnt lgkmcnt(0)
	global_load_dwordx4 v[66:69], v[70:71], off
	s_lshl_b32 s17, s22, 12
	s_and_b32 s17, s17, 0x3f000
	s_add_u32 s20, s33, s17
	s_addc_u32 s21, s53, 0
	s_ashr_i32 s17, s16, 31
	s_lshl_b64 s[24:25], s[16:17], 12
	s_add_u32 s24, s60, s24
	s_addc_u32 s25, s61, s25
	s_ashr_i32 s23, s22, 31
	s_lshl_b64 s[22:23], s[22:23], 12
	s_add_u32 s22, s60, s22
	v_lshlrev_b64 v[122:123], 1, v[142:143]
	s_addc_u32 s23, s61, s23
	s_waitcnt vmcnt(18)
	v_lshlrev_b32_e32 v72, 16, v74
	v_and_b32_e32 v73, 0xffff0000, v74
	v_lshlrev_b32_e32 v116, 16, v75
	v_and_b32_e32 v117, 0xffff0000, v75
	s_waitcnt vmcnt(14)
	v_lshlrev_b32_e32 v118, 16, v82
	v_and_b32_e32 v119, 0xffff0000, v82
	v_lshl_add_u64 v[166:167], s[24:25], 0, v[122:123]
	v_lshl_add_u64 v[168:169], s[22:23], 0, v[122:123]
	v_lshlrev_b32_e32 v120, 16, v83
	v_and_b32_e32 v121, 0xffff0000, v83
	s_mov_b64 s[22:23], 0x1000
	v_and_b32_e32 v180, 64, v202
	v_xor_b32_e32 v181, 1, v202
	v_add_u32_e32 v238, 64, v180
	v_readlane_b32 s76, v252, 9
	v_lshl_add_u64 v[212:213], v[170:171], 0, s[50:51]
	v_readlane_b32 s90, v252, 23
	v_readlane_b32 s91, v252, 24
	v_lshl_add_u64 v[184:185], s[42:43], 0, v[170:171]
	s_waitcnt vmcnt(0)
	v_lshlrev_b32_e32 v190, 16, v108
	v_lshl_add_u64 v[188:189], s[90:91], 0, v[170:171]
	v_and_b32_e32 v191, 0xffff0000, v108
	v_lshlrev_b32_e32 v192, 16, v109
	v_and_b32_e32 v193, 0xffff0000, v109
	v_lshlrev_b32_e32 v178, 16, v103
	v_and_b32_e32 v179, 0xffff0000, v103
	s_waitcnt vmcnt(0)
	v_lshlrev_b32_e32 v182, 16, v110
	v_and_b32_e32 v183, 0xffff0000, v110
	v_lshlrev_b32_e32 v186, 16, v111
	v_and_b32_e32 v187, 0xffff0000, v111
	v_xor_b32_e32 v207, 2, v202
	v_xor_b32_e32 v236, 4, v202
	v_xor_b32_e32 v211, 8, v202
	v_xor_b32_e32 v210, 16, v202
	v_xor_b32_e32 v237, 32, v202
	s_lshl_b64 s[16:17], s[16:17], 11
	v_lshl_add_u32 v209, v209, 3, 0
	s_add_i32 s73, s63, s65
	v_readlane_b32 s77, v252, 10
	v_readlane_b32 s78, v252, 11
	v_readlane_b32 s79, v252, 12
	v_readlane_b32 s80, v252, 13
	v_readlane_b32 s81, v252, 14
	v_readlane_b32 s82, v252, 15
	v_readlane_b32 s83, v252, 16
	v_readlane_b32 s84, v252, 17
	v_readlane_b32 s85, v252, 18
	v_readlane_b32 s86, v252, 19
	v_readlane_b32 s87, v252, 20
	v_readlane_b32 s88, v252, 21
	v_readlane_b32 s89, v252, 22
	s_waitcnt vmcnt(0)
	v_pk_add_f32 v[122:123], v[4:5], v[68:69]
	v_pk_add_f32 v[124:125], v[2:3], v[66:67]
	v_pk_add_f32 v[66:67], v[10:11], v[66:67]
	v_pk_add_f32 v[68:69], v[12:13], v[68:69]
	v_pk_add_f32 v[158:159], v[122:123], v[116:117]
	v_pk_add_f32 v[162:163], v[124:125], v[72:73]
	v_pk_add_f32 v[164:165], v[66:67], v[118:119]
	v_cvt_pk_bf16_f32 v248, v162, v163
	v_cvt_pk_bf16_f32 v249, v158, v159
	v_pk_add_f32 v[160:161], v[68:69], v[120:121]
	v_cvt_pk_bf16_f32 v250, v164, v165
	v_lshlrev_b32_e32 v72, 16, v76
	v_cvt_pk_bf16_f32 v251, v160, v161
	global_load_dwordx4 v[66:69], v[70:71], off offset:1024
	global_store_dwordx2 v[166:167], v[248:249], off
	global_store_dwordx2 v[168:169], v[250:251], off
	v_and_b32_e32 v73, 0xffff0000, v76
	v_lshlrev_b32_e32 v116, 16, v77
	v_and_b32_e32 v117, 0xffff0000, v77
	v_lshlrev_b32_e32 v118, 16, v84
	v_and_b32_e32 v119, 0xffff0000, v84
	v_lshlrev_b32_e32 v120, 16, v85
	v_and_b32_e32 v121, 0xffff0000, v85
	v_mov_b32_e32 v216, v163
	v_mov_b32_e32 v220, v159
	v_mov_b32_e32 v224, v165
	v_mov_b32_e32 v228, v161
	v_mov_b32_e32 v214, v162
	v_mov_b32_e32 v218, v158
	v_mov_b32_e32 v222, v164
	v_mov_b32_e32 v226, v160
	s_waitcnt vmcnt(2)
	v_pk_add_f32 v[122:123], v[8:9], v[68:69]
	v_pk_add_f32 v[124:125], v[6:7], v[66:67]
	v_pk_add_f32 v[66:67], v[14:15], v[66:67]
	v_pk_add_f32 v[68:69], v[16:17], v[68:69]
	v_pk_add_f32 v[150:151], v[122:123], v[116:117]
	v_pk_add_f32 v[152:153], v[124:125], v[72:73]
	v_pk_add_f32 v[156:157], v[66:67], v[118:119]
	v_cvt_pk_bf16_f32 v248, v152, v153
	v_cvt_pk_bf16_f32 v249, v150, v151
	v_pk_add_f32 v[154:155], v[68:69], v[120:121]
	v_cvt_pk_bf16_f32 v250, v156, v157
	v_lshlrev_b32_e32 v72, 16, v78
	v_cvt_pk_bf16_f32 v251, v154, v155
	global_load_dwordx4 v[66:69], v[70:71], off offset:2048
	global_store_dwordx2 v[166:167], v[248:249], off offset:512
	global_store_dwordx2 v[168:169], v[250:251], off offset:512
	v_and_b32_e32 v73, 0xffff0000, v78
	v_lshlrev_b32_e32 v116, 16, v79
	v_and_b32_e32 v117, 0xffff0000, v79
	v_lshlrev_b32_e32 v118, 16, v88
	v_and_b32_e32 v119, 0xffff0000, v88
	v_lshlrev_b32_e32 v120, 16, v89
	v_and_b32_e32 v121, 0xffff0000, v89
	v_mov_b32_e32 v217, v153
	v_mov_b32_e32 v221, v151
	v_mov_b32_e32 v225, v157
	v_mov_b32_e32 v229, v155
	v_mov_b32_e32 v215, v152
	v_mov_b32_e32 v219, v150
	v_mov_b32_e32 v223, v156
	v_mov_b32_e32 v227, v154
	s_waitcnt vmcnt(2)
	v_pk_add_f32 v[122:123], v[20:21], v[68:69]
	v_pk_add_f32 v[124:125], v[18:19], v[66:67]
	v_pk_add_f32 v[66:67], v[26:27], v[66:67]
	v_pk_add_f32 v[68:69], v[28:29], v[68:69]
	v_pk_add_f32 v[140:141], v[122:123], v[116:117]
	v_pk_add_f32 v[144:145], v[124:125], v[72:73]
	v_pk_add_f32 v[148:149], v[66:67], v[118:119]
	v_cvt_pk_bf16_f32 v248, v144, v145
	v_cvt_pk_bf16_f32 v249, v140, v141
	v_pk_add_f32 v[146:147], v[68:69], v[120:121]
	v_cvt_pk_bf16_f32 v250, v148, v149
	v_lshl_add_u64 v[120:121], v[170:171], 0, s[22:23]
	v_cvt_pk_bf16_f32 v251, v146, v147
	global_load_dwordx4 v[66:69], v[70:71], off offset:3072
	global_store_dwordx2 v[166:167], v[248:249], off offset:1024
	global_store_dwordx2 v[168:169], v[250:251], off offset:1024
	v_lshl_add_u64 v[122:123], s[18:19], 0, v[120:121]
	v_lshlrev_b32_e32 v70, 16, v80
	v_and_b32_e32 v71, 0xffff0000, v80
	v_lshlrev_b32_e32 v72, 16, v81
	v_and_b32_e32 v73, 0xffff0000, v81
	v_lshlrev_b32_e32 v116, 16, v90
	v_and_b32_e32 v117, 0xffff0000, v90
	v_add_co_u32_e32 v122, vcc, s66, v122
	v_lshlrev_b32_e32 v118, 16, v91
	v_and_b32_e32 v119, 0xffff0000, v91
	v_addc_co_u32_e32 v123, vcc, 0, v123, vcc
	v_lshl_add_u64 v[120:121], s[20:21], 0, v[120:121]
	s_waitcnt vmcnt(2)
	v_pk_add_f32 v[124:125], v[24:25], v[68:69]
	v_pk_add_f32 v[126:127], v[22:23], v[66:67]
	v_pk_add_f32 v[66:67], v[30:31], v[66:67]
	v_pk_add_f32 v[68:69], v[32:33], v[68:69]
	v_pk_add_f32 v[132:133], v[124:125], v[72:73]
	v_pk_add_f32 v[136:137], v[126:127], v[70:71]
	v_pk_add_f32 v[138:139], v[66:67], v[116:117]
	v_cvt_pk_bf16_f32 v248, v136, v137
	v_cvt_pk_bf16_f32 v249, v132, v133
	v_pk_add_f32 v[134:135], v[68:69], v[118:119]
	v_cvt_pk_bf16_f32 v250, v138, v139
	v_add_co_u32_e32 v70, vcc, s66, v120
	v_cvt_pk_bf16_f32 v251, v134, v135
	global_load_dwordx4 v[66:69], v[122:123], off
	v_addc_co_u32_e32 v71, vcc, 0, v121, vcc
	global_load_dwordx4 v[70:73], v[70:71], off
	global_store_dwordx2 v[166:167], v[248:249], off offset:1536
	global_store_dwordx2 v[168:169], v[250:251], off offset:1536
	v_lshl_add_u64 v[124:125], v[170:171], 0, s[46:47]
	v_lshl_add_u64 v[126:127], s[18:19], 0, v[124:125]
	v_lshlrev_b32_e32 v116, 16, v94
	v_and_b32_e32 v117, 0xffff0000, v94
	v_lshlrev_b32_e32 v118, 16, v95
	v_and_b32_e32 v119, 0xffff0000, v95
	v_add_co_u32_e32 v172, vcc, s66, v126
	v_lshlrev_b32_e32 v120, 16, v104
	v_and_b32_e32 v121, 0xffff0000, v104
	v_lshlrev_b32_e32 v122, 16, v105
	v_and_b32_e32 v123, 0xffff0000, v105
	v_addc_co_u32_e32 v173, vcc, 0, v127, vcc
	v_lshl_add_u64 v[174:175], s[20:21], 0, v[124:125]
	s_waitcnt vmcnt(3)
	v_pk_add_f32 v[68:69], v[36:37], v[68:69]
	v_pk_add_f32 v[66:67], v[34:35], v[66:67]
	v_pk_add_f32 v[124:125], v[68:69], v[118:119]
	s_waitcnt vmcnt(2)
	v_pk_add_f32 v[72:73], v[40:41], v[72:73]
	v_pk_add_f32 v[70:71], v[38:39], v[70:71]
	v_pk_add_f32 v[128:129], v[66:67], v[116:117]
	v_pk_add_f32 v[126:127], v[72:73], v[122:123]
	v_cvt_pk_bf16_f32 v248, v128, v129
	v_cvt_pk_bf16_f32 v249, v124, v125
	v_pk_add_f32 v[130:131], v[70:71], v[120:121]
	v_add_co_u32_e32 v70, vcc, s66, v174
	v_cvt_pk_bf16_f32 v250, v130, v131
	v_cvt_pk_bf16_f32 v251, v126, v127
	global_load_dwordx4 v[66:69], v[172:173], off
	v_addc_co_u32_e32 v71, vcc, 0, v175, vcc
	global_load_dwordx4 v[70:73], v[70:71], off
	global_store_dwordx2 v[166:167], v[248:249], off offset:2048
	global_store_dwordx2 v[168:169], v[250:251], off offset:2048
	v_lshl_add_u64 v[120:121], v[170:171], 0, s[48:49]
	v_lshl_add_u64 v[174:175], s[18:19], 0, v[120:121]
	v_lshlrev_b32_e32 v118, 16, v96
	v_and_b32_e32 v119, 0xffff0000, v96
	v_lshlrev_b32_e32 v116, 16, v97
	v_and_b32_e32 v117, 0xffff0000, v97
	v_add_co_u32_e32 v174, vcc, s66, v174
	v_lshlrev_b32_e32 v122, 16, v106
	v_and_b32_e32 v123, 0xffff0000, v106
	v_lshlrev_b32_e32 v172, 16, v107
	v_and_b32_e32 v173, 0xffff0000, v107
	v_addc_co_u32_e32 v175, vcc, 0, v175, vcc
	v_lshl_add_u64 v[176:177], s[20:21], 0, v[120:121]
	s_waitcnt vmcnt(3)
	v_pk_add_f32 v[68:69], v[44:45], v[68:69]
	v_pk_add_f32 v[66:67], v[42:43], v[66:67]
	v_pk_add_f32 v[116:117], v[68:69], v[116:117]
	s_waitcnt vmcnt(2)
	v_pk_add_f32 v[72:73], v[48:49], v[72:73]
	v_pk_add_f32 v[70:71], v[46:47], v[70:71]
	v_pk_add_f32 v[120:121], v[66:67], v[118:119]
	v_pk_add_f32 v[118:119], v[72:73], v[172:173]
	v_cvt_pk_bf16_f32 v248, v120, v121
	v_cvt_pk_bf16_f32 v249, v116, v117
	v_pk_add_f32 v[122:123], v[70:71], v[122:123]
	v_add_co_u32_e32 v70, vcc, s66, v176
	v_cvt_pk_bf16_f32 v250, v122, v123
	v_cvt_pk_bf16_f32 v251, v118, v119
	global_load_dwordx4 v[66:69], v[174:175], off
	v_addc_co_u32_e32 v71, vcc, 0, v177, vcc
	global_load_dwordx4 v[70:73], v[70:71], off
	global_store_dwordx2 v[166:167], v[248:249], off offset:2560
	global_store_dwordx2 v[168:169], v[250:251], off offset:2560
	v_cmp_lt_i32_e32 vcc, v181, v238
	v_lshlrev_b32_e32 v174, 16, v98
	v_and_b32_e32 v175, 0xffff0000, v98
	v_cndmask_b32_e32 v180, v202, v181, vcc
	v_lshlrev_b32_e32 v208, 2, v180
	v_lshl_add_u64 v[180:181], s[44:45], 0, v[170:171]
	v_lshl_add_u64 v[170:171], s[18:19], 0, v[212:213]
	v_lshlrev_b32_e32 v176, 16, v99
	v_and_b32_e32 v177, 0xffff0000, v99
	v_add_co_u32_e32 v170, vcc, s66, v170
	v_lshl_add_u64 v[212:213], s[20:21], 0, v[212:213]
	s_nop 0
	v_addc_co_u32_e32 v171, vcc, 0, v171, vcc
	v_add_co_u32_e32 v212, vcc, s66, v212
	v_lshlrev_b32_e32 v172, 16, v102
	s_nop 0
	v_addc_co_u32_e32 v213, vcc, 0, v213, vcc
	v_and_b32_e32 v173, 0xffff0000, v102
	v_cmp_lt_i32_e32 vcc, v207, v238
	s_mul_i32 s18, s97, 0x2020
	s_waitcnt vmcnt(3)
	v_pk_add_f32 v[68:69], v[52:53], v[68:69]
	v_pk_add_f32 v[66:67], v[50:51], v[66:67]
	s_waitcnt vmcnt(2)
	v_pk_add_f32 v[72:73], v[56:57], v[72:73]
	v_pk_add_f32 v[230:231], v[54:55], v[70:71]
	v_pk_add_f32 v[70:71], v[68:69], v[176:177]
	v_pk_add_f32 v[174:175], v[66:67], v[174:175]
	v_pk_add_f32 v[72:73], v[72:73], v[192:193]
	v_cvt_pk_bf16_f32 v66, v174, v175
	v_cvt_pk_bf16_f32 v67, v70, v71
	v_pk_add_f32 v[176:177], v[230:231], v[190:191]
	s_nop 0
	v_cvt_pk_bf16_f32 v68, v176, v177
	v_cvt_pk_bf16_f32 v69, v72, v73
	global_store_dwordx2 v[166:167], v[66:67], off offset:3072
	global_store_dwordx2 v[168:169], v[68:69], off offset:3072
	global_load_dwordx4 v[66:69], v[170:171], off
	s_nop 0
	global_load_dwordx4 v[190:193], v[212:213], off
	v_pk_mul_f32 v[170:171], v[216:217], v[216:217]
	v_pk_mul_f32 v[212:213], v[220:221], v[220:221]
	v_pk_mul_f32 v[216:217], v[224:225], v[224:225]
	v_pk_mul_f32 v[220:221], v[228:229], v[228:229]
	v_pk_fma_f32 v[170:171], v[214:215], v[214:215], v[170:171]
	v_pk_fma_f32 v[212:213], v[218:219], v[218:219], v[212:213]
	v_pk_fma_f32 v[214:215], v[222:223], v[222:223], v[216:217]
	v_pk_fma_f32 v[216:217], v[226:227], v[226:227], v[220:221]
	v_pk_add_f32 v[170:171], v[170:171], v[212:213]
	v_pk_add_f32 v[212:213], v[214:215], v[216:217]
	v_pk_mul_f32 v[214:215], v[140:141], v[140:141]
	v_pk_mul_f32 v[216:217], v[144:145], v[144:145]
	v_pk_mul_f32 v[218:219], v[146:147], v[146:147]
	v_pk_mul_f32 v[220:221], v[148:149], v[148:149]
	v_pk_mov_b32 v[222:223], v[216:217], v[214:215] op_sel:[1,0]
	v_mov_b32_e32 v217, v215
	v_pk_mov_b32 v[214:215], v[220:221], v[218:219] op_sel:[1,0]
	v_mov_b32_e32 v221, v219
	v_pk_add_f32 v[216:217], v[222:223], v[216:217]
	v_mul_f32_e32 v222, v139, v139
	v_mul_f32_e32 v224, v135, v135
	v_pk_add_f32 v[214:215], v[214:215], v[220:221]
	v_mul_f32_e32 v218, v137, v137
	v_mul_f32_e32 v220, v133, v133
	v_pk_fma_f32 v[222:223], v[138:139], v[138:139], v[222:223] op_sel_hi:[1,1,0]
	v_pk_fma_f32 v[224:225], v[134:135], v[134:135], v[224:225] op_sel_hi:[1,1,0]
	v_pk_add_f32 v[170:171], v[170:171], v[170:171] op_sel:[0,1] op_sel_hi:[1,0]
	v_pk_add_f32 v[212:213], v[212:213], v[212:213] op_sel:[0,1] op_sel_hi:[1,0]
	v_pk_add_f32 v[216:217], v[216:217], v[216:217] op_sel:[0,1] op_sel_hi:[1,0]
	v_pk_add_f32 v[214:215], v[214:215], v[214:215] op_sel:[0,1] op_sel_hi:[1,0]
	v_pk_fma_f32 v[218:219], v[136:137], v[136:137], v[218:219] op_sel_hi:[1,1,0]
	v_pk_fma_f32 v[220:221], v[132:133], v[132:133], v[220:221] op_sel_hi:[1,1,0]
	v_mul_f32_e32 v223, v130, v130
	v_mul_f32_e32 v225, v131, v131
	v_mul_f32_e32 v226, v126, v126
	v_mul_f32_e32 v227, v127, v127
	v_mul_f32_e32 v171, v128, v128
	v_mul_f32_e32 v217, v129, v129
	v_mul_f32_e32 v219, v124, v124
	v_mul_f32_e32 v221, v125, v125
	v_mov_b32_e32 v213, v223
	v_mov_b32_e32 v215, v225
	v_mov_b32_e32 v223, v226
	v_mov_b32_e32 v225, v227
	v_pk_add_f32 v[170:171], v[170:171], v[216:217]
	v_pk_add_f32 v[216:217], v[218:219], v[220:221]
	v_pk_add_f32 v[212:213], v[212:213], v[214:215]
	v_pk_add_f32 v[214:215], v[222:223], v[224:225]
	v_pk_add_f32 v[170:171], v[170:171], v[216:217]
	v_pk_add_f32 v[212:213], v[212:213], v[214:215]
	v_pk_add_f32 v[220:221], v[170:171], v[170:171] op_sel:[0,1] op_sel_hi:[1,0]
	v_pk_add_f32 v[222:223], v[212:213], v[212:213] op_sel:[0,1] op_sel_hi:[1,0]
	v_pk_mul_f32 v[170:171], v[116:117], v[116:117]
	v_pk_mul_f32 v[212:213], v[120:121], v[120:121]
	v_pk_mul_f32 v[214:215], v[118:119], v[118:119]
	v_pk_mul_f32 v[216:217], v[122:123], v[122:123]
	v_pk_mov_b32 v[218:219], v[212:213], v[170:171] op_sel:[1,0]
	v_mov_b32_e32 v213, v171
	v_pk_mov_b32 v[170:171], v[216:217], v[214:215] op_sel:[1,0]
	v_mov_b32_e32 v217, v215
	v_pk_add_f32 v[170:171], v[170:171], v[216:217]
	v_pk_add_f32 v[212:213], v[218:219], v[212:213]
	v_pk_add_f32 v[226:227], v[170:171], v[170:171] op_sel:[0,1] op_sel_hi:[1,0]
	v_mul_f32_e32 v170, v175, v175
	v_pk_fma_f32 v[228:229], v[174:175], v[174:175], v[170:171] op_sel_hi:[1,1,0]
	v_pk_add_f32 v[224:225], v[212:213], v[212:213] op_sel:[0,1] op_sel_hi:[1,0]
	v_mul_f32_e32 v212, v71, v71
	v_mul_f32_e32 v214, v177, v177
	v_mul_f32_e32 v216, v73, v73
	v_pk_fma_f32 v[230:231], v[70:71], v[70:71], v[212:213] op_sel_hi:[1,1,0]
	v_pk_fma_f32 v[232:233], v[176:177], v[176:177], v[214:215] op_sel_hi:[1,1,0]
	v_pk_fma_f32 v[234:235], v[72:73], v[72:73], v[216:217] op_sel_hi:[1,1,0]
	s_waitcnt vmcnt(1)
	v_pk_add_f32 v[68:69], v[60:61], v[68:69]
	v_pk_add_f32 v[170:171], v[58:59], v[66:67]
	s_waitcnt vmcnt(0)
	v_pk_add_f32 v[192:193], v[64:65], v[192:193]
	v_pk_add_f32 v[190:191], v[62:63], v[190:191]
	v_pk_add_f32 v[66:67], v[68:69], v[178:179]
	v_pk_add_f32 v[170:171], v[170:171], v[172:173]
	v_pk_add_f32 v[68:69], v[192:193], v[186:187]
	v_cvt_pk_bf16_f32 v178, v170, v171
	v_cvt_pk_bf16_f32 v179, v66, v67
	v_pk_add_f32 v[172:173], v[190:191], v[182:183]
	v_mul_f32_e32 v221, v170, v170
	v_cvt_pk_bf16_f32 v182, v172, v173
	v_cvt_pk_bf16_f32 v183, v68, v69
	global_store_dwordx2 v[166:167], v[178:179], off offset:3584
	global_store_dwordx2 v[168:169], v[182:183], off offset:3584
	global_load_dwordx4 v[190:193], v[184:185], off
	global_load_dwordx4 v[212:215], v[188:189], off
	global_load_dwordx4 v[216:219], v[180:181], off
	v_mul_f32_e32 v225, v171, v171
	v_mul_f32_e32 v229, v66, v66
	v_mul_f32_e32 v231, v67, v67
	v_mul_f32_e32 v223, v172, v172
	v_mul_f32_e32 v227, v173, v173
	v_mul_f32_e32 v233, v68, v68
	v_mul_f32_e32 v235, v69, v69
	v_pk_add_f32 v[166:167], v[220:221], v[224:225]
	v_pk_add_f32 v[168:169], v[228:229], v[230:231]
	v_pk_add_f32 v[178:179], v[222:223], v[226:227]
	v_pk_add_f32 v[182:183], v[232:233], v[234:235]
	v_pk_add_f32 v[166:167], v[166:167], v[168:169]
	v_pk_add_f32 v[168:169], v[178:179], v[182:183]
	v_mov_b32_e32 v179, v166
	v_mov_b32_e32 v178, v168
	v_mov_b32_e32 v166, v169
	v_pk_add_f32 v[166:167], v[178:179], v[166:167]
	ds_bpermute_b32 v179, v208, v167
	ds_bpermute_b32 v178, v208, v166
	v_cndmask_b32_e32 v168, v202, v207, vcc
	v_lshlrev_b32_e32 v169, 2, v168
	v_cmp_lt_i32_e32 vcc, v236, v238
	v_lshl_add_u64 v[220:221], s[34:35], 0, v[142:143]
	s_waitcnt lgkmcnt(0)
	v_pk_add_f32 v[166:167], v[166:167], v[178:179]
	ds_bpermute_b32 v183, v169, v167
	ds_bpermute_b32 v182, v169, v166
	v_cndmask_b32_e32 v168, v202, v236, vcc
	v_lshlrev_b32_e32 v179, 2, v168
	v_cmp_lt_i32_e32 vcc, v211, v238
	v_lshl_add_u64 v[142:143], v[220:221], 0, s[16:17]
	s_waitcnt lgkmcnt(0)
	v_pk_add_f32 v[166:167], v[166:167], v[182:183]
	ds_bpermute_b32 v187, v179, v167
	ds_bpermute_b32 v186, v179, v166
	v_cndmask_b32_e32 v168, v202, v211, vcc
	v_lshlrev_b32_e32 v182, 2, v168
	v_cmp_lt_i32_e32 vcc, v210, v238
	v_mov_b32_e32 v222, 0
	s_waitcnt lgkmcnt(0)
	v_pk_add_f32 v[166:167], v[166:167], v[186:187]
	ds_bpermute_b32 v187, v182, v167
	ds_bpermute_b32 v186, v182, v166
	v_cndmask_b32_e32 v168, v202, v210, vcc
	v_lshlrev_b32_e32 v183, 2, v168
	v_cmp_lt_i32_e32 vcc, v237, v238
	v_mov_b32_e32 v207, 0
	s_waitcnt lgkmcnt(0)
	v_pk_add_f32 v[166:167], v[166:167], v[186:187]
	ds_bpermute_b32 v211, v183, v167
	ds_bpermute_b32 v210, v183, v166
	v_cndmask_b32_e32 v178, v202, v237, vcc
	v_lshlrev_b32_e32 v186, 2, v178
	v_add_u32_e32 v187, s18, v209
	s_add_i32 s18, s63, s64
	s_waitcnt lgkmcnt(0)
	v_pk_add_f32 v[166:167], v[166:167], v[210:211]
	ds_bpermute_b32 v211, v186, v167
	ds_bpermute_b32 v210, v186, v166
	s_ashr_i32 s19, s18, 31
	s_lshl_b64 s[18:19], s[18:19], 11
	s_cmpk_gt_i32 s73, 0x3fff
	s_cselect_b64 s[56:57], -1, 0
	s_waitcnt lgkmcnt(0)
	v_pk_add_f32 v[166:167], v[166:167], v[210:211]
	s_waitcnt vmcnt(2)
	v_pk_add_f32 v[190:191], v[190:191], 1.0 op_sel_hi:[1,0]
	v_pk_fma_f32 v[166:167], v[166:167], s[52:53], v[114:115] op_sel_hi:[1,0,0]
	s_waitcnt vmcnt(1)
	v_pk_mul_f32 v[190:191], v[212:213], v[190:191]
	v_mul_f32_e32 v168, 0x4b800000, v167
	v_cmp_gt_f32_e32 vcc, s67, v167
	v_mul_f32_e32 v178, 0x4b800000, v166
	v_cmp_gt_f32_e64 s[16:17], s67, v166
	v_cndmask_b32_e32 v167, v167, v168, vcc
	v_rsq_f32_e32 v168, v167
	v_cndmask_b32_e64 v166, v166, v178, s[16:17]
	v_rsq_f32_e32 v210, v166
	v_pk_add_f32 v[192:193], v[192:193], 1.0 op_sel_hi:[1,0]
	v_mul_f32_e32 v178, 0x45800000, v168
	v_cndmask_b32_e32 v178, v168, v178, vcc
	v_mul_f32_e32 v211, 0x45800000, v210
	v_cndmask_b32_e64 v168, v210, v211, s[16:17]
	v_pk_mul_f32 v[162:163], v[162:163], v[178:179] op_sel_hi:[1,0]
	v_pk_mul_f32 v[164:165], v[164:165], v[168:169] op_sel_hi:[1,0]
	s_waitcnt vmcnt(0)
	v_pk_fma_f32 v[162:163], v[190:191], v[162:163], v[216:217]
	v_pk_mul_f32 v[158:159], v[158:159], v[178:179] op_sel_hi:[1,0]
	v_pk_mul_f32 v[160:161], v[160:161], v[168:169] op_sel_hi:[1,0]
	v_pk_mul_f32 v[192:193], v[214:215], v[192:193]
	v_pk_fma_f32 v[164:165], v[190:191], v[164:165], v[216:217]
	v_cvt_pk_bf16_f32 v190, v162, v163
	v_med3_f32 v162, v162, s68, v203
	v_med3_f32 v163, v163, s68, v203
	v_pk_fma_f32 v[158:159], v[192:193], v[158:159], v[218:219]
	v_pk_fma_f32 v[160:161], v[192:193], v[160:161], v[218:219]
	v_med3_f32 v192, v164, s68, v203
	v_cvt_pk_fp8_f32 v222, v162, v163
	v_med3_f32 v162, v165, s68, v203
	v_cvt_pk_fp8_f32 v207, v192, v162
	v_cvt_pk_bf16_f32 v191, v158, v159
	v_med3_f32 v158, v158, s68, v203
	v_med3_f32 v159, v159, s68, v203
	v_med3_f32 v163, v160, s68, v203
	v_cvt_pk_fp8_f32 v222, v158, v159 op_sel:[0,0,1]
	v_med3_f32 v158, v161, s68, v203
	v_cvt_pk_fp8_f32 v207, v163, v158 op_sel:[0,0,1]
	v_lshl_add_u64 v[166:167], v[220:221], 0, s[18:19]
	ds_write_b64 v187, v[190:191]
	global_store_dword v[142:143], v222, off
	v_cvt_pk_bf16_f32 v164, v164, v165
	v_cvt_pk_bf16_f32 v165, v160, v161
	global_store_dword v[166:167], v207, off
	global_load_dwordx4 v[160:163], v[184:185], off offset:1024
	global_load_dwordx4 v[190:193], v[188:189], off offset:1024
	global_load_dwordx4 v[210:213], v[180:181], off offset:1024
	s_mul_i32 s16, s64, 0x1010
	v_pk_mul_f32 v[152:153], v[152:153], v[178:179] op_sel_hi:[1,0]
	v_add_u32_e32 v158, s16, v209
	v_pk_mul_f32 v[156:157], v[156:157], v[168:169] op_sel_hi:[1,0]
	v_mov_b32_e32 v159, 0
	v_pk_mul_f32 v[150:151], v[150:151], v[178:179] op_sel_hi:[1,0]
	v_pk_mul_f32 v[154:155], v[154:155], v[168:169] op_sel_hi:[1,0]
	ds_write_b64 v158, v[164:165]
	v_mov_b32_e32 v207, 0
	v_pk_mul_f32 v[144:145], v[144:145], v[178:179] op_sel_hi:[1,0]
	v_pk_mul_f32 v[148:149], v[148:149], v[168:169] op_sel_hi:[1,0]
	v_pk_mul_f32 v[140:141], v[140:141], v[178:179] op_sel_hi:[1,0]
	v_pk_mul_f32 v[146:147], v[146:147], v[168:169] op_sel_hi:[1,0]
	v_pk_mul_f32 v[136:137], v[136:137], v[178:179] op_sel_hi:[1,0]
	v_pk_mul_f32 v[138:139], v[138:139], v[168:169] op_sel_hi:[1,0]
	v_pk_mul_f32 v[132:133], v[132:133], v[178:179] op_sel_hi:[1,0]
	v_pk_mul_f32 v[134:135], v[134:135], v[168:169] op_sel_hi:[1,0]
	v_pk_mul_f32 v[128:129], v[128:129], v[178:179] op_sel_hi:[1,0]
	v_pk_mul_f32 v[130:131], v[130:131], v[168:169] op_sel_hi:[1,0]
	v_pk_mul_f32 v[124:125], v[124:125], v[178:179] op_sel_hi:[1,0]
	v_pk_mul_f32 v[126:127], v[126:127], v[168:169] op_sel_hi:[1,0]
	v_pk_mul_f32 v[120:121], v[120:121], v[178:179] op_sel_hi:[1,0]
	v_pk_mul_f32 v[122:123], v[122:123], v[168:169] op_sel_hi:[1,0]
	v_pk_mul_f32 v[116:117], v[116:117], v[178:179] op_sel_hi:[1,0]
	v_pk_mul_f32 v[118:119], v[118:119], v[168:169] op_sel_hi:[1,0]
	v_pk_mul_f32 v[70:71], v[70:71], v[178:179] op_sel_hi:[1,0]
	v_pk_mul_f32 v[72:73], v[72:73], v[168:169] op_sel_hi:[1,0]
	v_pk_mul_f32 v[66:67], v[66:67], v[178:179] op_sel_hi:[1,0]
	v_pk_mul_f32 v[68:69], v[68:69], v[168:169] op_sel_hi:[1,0]
	s_waitcnt vmcnt(2)
	v_pk_add_f32 v[160:161], v[160:161], 1.0 op_sel_hi:[1,0]
	s_waitcnt vmcnt(1)
	v_pk_mul_f32 v[160:161], v[190:191], v[160:161]
	v_pk_add_f32 v[162:163], v[162:163], 1.0 op_sel_hi:[1,0]
	s_waitcnt vmcnt(0)
	v_pk_fma_f32 v[152:153], v[152:153], v[160:161], v[210:211]
	v_pk_mul_f32 v[162:163], v[192:193], v[162:163]
	v_pk_fma_f32 v[156:157], v[156:157], v[160:161], v[210:211]
	v_cvt_pk_bf16_f32 v160, v152, v153
	v_med3_f32 v152, v152, s68, v203
	v_med3_f32 v153, v153, s68, v203
	v_pk_fma_f32 v[150:151], v[150:151], v[162:163], v[212:213]
	v_pk_fma_f32 v[154:155], v[154:155], v[162:163], v[212:213]
	v_med3_f32 v162, v156, s68, v203
	v_cvt_pk_fp8_f32 v159, v152, v153
	v_med3_f32 v152, v157, s68, v203
	v_cvt_pk_fp8_f32 v207, v162, v152
	v_cvt_pk_bf16_f32 v161, v150, v151
	v_med3_f32 v150, v150, s68, v203
	v_med3_f32 v151, v151, s68, v203
	v_med3_f32 v153, v154, s68, v203
	v_cvt_pk_fp8_f32 v159, v150, v151 op_sel:[0,0,1]
	v_med3_f32 v150, v155, s68, v203
	v_cvt_pk_fp8_f32 v207, v153, v150 op_sel:[0,0,1]
	ds_write_b64 v187, v[160:161] offset:512
	global_store_dword v[142:143], v159, off offset:256
	v_cvt_pk_bf16_f32 v164, v156, v157
	v_cvt_pk_bf16_f32 v165, v154, v155
	global_store_dword v[166:167], v207, off offset:256
	global_load_dwordx4 v[150:153], v[184:185], off offset:2048
	global_load_dwordx4 v[154:157], v[188:189], off offset:2048
	global_load_dwordx4 v[160:163], v[180:181], off offset:2048
	v_mov_b32_e32 v159, 0
	ds_write_b64 v158, v[164:165] offset:512
	v_mov_b32_e32 v190, 0
	s_waitcnt vmcnt(2)
	v_pk_add_f32 v[150:151], v[150:151], 1.0 op_sel_hi:[1,0]
	s_waitcnt vmcnt(1)
	v_pk_mul_f32 v[150:151], v[154:155], v[150:151]
	v_pk_add_f32 v[152:153], v[152:153], 1.0 op_sel_hi:[1,0]
	s_waitcnt vmcnt(0)
	v_pk_fma_f32 v[144:145], v[144:145], v[150:151], v[160:161]
	v_pk_mul_f32 v[152:153], v[156:157], v[152:153]
	v_pk_fma_f32 v[148:149], v[148:149], v[150:151], v[160:161]
	v_cvt_pk_bf16_f32 v150, v144, v145
	v_med3_f32 v144, v144, s68, v203
	v_med3_f32 v145, v145, s68, v203
	v_pk_fma_f32 v[140:141], v[140:141], v[152:153], v[162:163]
	v_pk_fma_f32 v[146:147], v[146:147], v[152:153], v[162:163]
	v_med3_f32 v152, v148, s68, v203
	v_cvt_pk_fp8_f32 v159, v144, v145
	v_med3_f32 v144, v149, s68, v203
	v_cvt_pk_fp8_f32 v190, v152, v144
	v_cvt_pk_bf16_f32 v151, v140, v141
	v_med3_f32 v140, v140, s68, v203
	v_med3_f32 v141, v141, s68, v203
	v_med3_f32 v145, v146, s68, v203
	v_cvt_pk_fp8_f32 v159, v140, v141 op_sel:[0,0,1]
	v_med3_f32 v140, v147, s68, v203
	v_cvt_pk_fp8_f32 v190, v145, v140 op_sel:[0,0,1]
	ds_write_b64 v187, v[150:151] offset:1024
	global_store_dword v[142:143], v159, off offset:512
	v_cvt_pk_bf16_f32 v160, v148, v149
	v_cvt_pk_bf16_f32 v161, v146, v147
	global_store_dword v[166:167], v190, off offset:512
	global_load_dwordx4 v[146:149], v[184:185], off offset:3072
	global_load_dwordx4 v[150:153], v[188:189], off offset:3072
	global_load_dwordx4 v[154:157], v[180:181], off offset:3072
	v_mov_b32_e32 v159, 0
	ds_write_b64 v158, v[160:161] offset:1024
	v_mov_b32_e32 v162, 0
	v_add_co_u32_e32 v140, vcc, s69, v188
	s_waitcnt vmcnt(2)
	v_pk_add_f32 v[146:147], v[146:147], 1.0 op_sel_hi:[1,0]
	s_waitcnt vmcnt(1)
	v_pk_mul_f32 v[146:147], v[150:151], v[146:147]
	v_pk_add_f32 v[148:149], v[148:149], 1.0 op_sel_hi:[1,0]
	s_waitcnt vmcnt(0)
	v_pk_fma_f32 v[136:137], v[136:137], v[146:147], v[154:155]
	v_pk_mul_f32 v[148:149], v[152:153], v[148:149]
	v_pk_fma_f32 v[138:139], v[138:139], v[146:147], v[154:155]
	v_cvt_pk_bf16_f32 v146, v136, v137
	v_med3_f32 v136, v136, s68, v203
	v_med3_f32 v137, v137, s68, v203
	v_pk_fma_f32 v[132:133], v[132:133], v[148:149], v[156:157]
	v_pk_fma_f32 v[134:135], v[134:135], v[148:149], v[156:157]
	v_med3_f32 v148, v138, s68, v203
	v_cvt_pk_fp8_f32 v159, v136, v137
	v_med3_f32 v136, v139, s68, v203
	v_cvt_pk_fp8_f32 v162, v148, v136
	v_cvt_pk_bf16_f32 v147, v132, v133
	v_med3_f32 v132, v132, s68, v203
	v_med3_f32 v133, v133, s68, v203
	v_med3_f32 v137, v134, s68, v203
	v_cvt_pk_fp8_f32 v159, v132, v133 op_sel:[0,0,1]
	v_med3_f32 v132, v135, s68, v203
	v_cvt_pk_fp8_f32 v162, v137, v132 op_sel:[0,0,1]
	v_addc_co_u32_e32 v141, vcc, 0, v189, vcc
	v_add_co_u32_e32 v144, vcc, s69, v184
	ds_write_b64 v187, v[146:147] offset:1536
	s_nop 0
	v_addc_co_u32_e32 v145, vcc, 0, v185, vcc
	global_store_dword v[142:143], v159, off offset:768
	v_cvt_pk_bf16_f32 v138, v138, v139
	v_cvt_pk_bf16_f32 v139, v134, v135
	global_store_dword v[166:167], v162, off offset:768
	global_load_dwordx4 v[134:137], v[140:141], off
	global_load_dwordx4 v[146:149], v[144:145], off
	v_add_co_u32_e32 v132, vcc, s69, v180
	ds_write_b64 v158, v[138:139] offset:1536
	s_nop 0
	v_addc_co_u32_e32 v133, vcc, 0, v181, vcc
	global_load_dwordx4 v[150:153], v[132:133], off
	v_mov_b32_e32 v154, 0
	v_mov_b32_e32 v155, 0
	s_and_b64 vcc, exec, s[56:57]
	s_waitcnt vmcnt(1)
	v_pk_add_f32 v[146:147], v[146:147], 1.0 op_sel_hi:[1,0]
	s_nop 0
	v_pk_mul_f32 v[134:135], v[134:135], v[146:147]
	v_pk_add_f32 v[138:139], v[148:149], 1.0 op_sel_hi:[1,0]
	v_mov_b32_e32 v146, 0
	v_pk_mul_f32 v[136:137], v[136:137], v[138:139]
	v_mov_b32_e32 v147, 0
	s_waitcnt vmcnt(0)
	v_pk_fma_f32 v[128:129], v[128:129], v[134:135], v[150:151]
	v_pk_fma_f32 v[130:131], v[130:131], v[134:135], v[150:151]
	v_cvt_pk_bf16_f32 v134, v128, v129
	v_med3_f32 v128, v128, s68, v203
	v_med3_f32 v129, v129, s68, v203
	v_pk_fma_f32 v[124:125], v[124:125], v[136:137], v[152:153]
	v_pk_fma_f32 v[126:127], v[126:127], v[136:137], v[152:153]
	v_med3_f32 v136, v130, s68, v203
	v_cvt_pk_fp8_f32 v154, v128, v129
	v_med3_f32 v128, v131, s68, v203
	v_cvt_pk_fp8_f32 v155, v136, v128
	v_cvt_pk_bf16_f32 v135, v124, v125
	v_med3_f32 v124, v124, s68, v203
	v_med3_f32 v125, v125, s68, v203
	v_med3_f32 v129, v126, s68, v203
	v_cvt_pk_fp8_f32 v154, v124, v125 op_sel:[0,0,1]
	v_med3_f32 v124, v127, s68, v203
	v_cvt_pk_fp8_f32 v155, v129, v124 op_sel:[0,0,1]
	ds_write_b64 v187, v[134:135] offset:2048
	global_store_dword v[142:143], v154, off offset:1024
	v_cvt_pk_bf16_f32 v138, v130, v131
	v_cvt_pk_bf16_f32 v139, v126, v127
	global_store_dword v[166:167], v155, off offset:1024
	global_load_dwordx4 v[124:127], v[144:145], off offset:1024
	global_load_dwordx4 v[128:131], v[140:141], off offset:1024
	global_load_dwordx4 v[134:137], v[132:133], off offset:1024
	ds_write_b64 v158, v[138:139] offset:2048
	s_waitcnt vmcnt(2)
	v_pk_add_f32 v[124:125], v[124:125], 1.0 op_sel_hi:[1,0]
	s_waitcnt vmcnt(1)
	v_pk_mul_f32 v[124:125], v[128:129], v[124:125]
	v_pk_add_f32 v[126:127], v[126:127], 1.0 op_sel_hi:[1,0]
	s_waitcnt vmcnt(0)
	v_pk_fma_f32 v[120:121], v[120:121], v[124:125], v[134:135]
	v_pk_mul_f32 v[126:127], v[130:131], v[126:127]
	v_pk_fma_f32 v[122:123], v[122:123], v[124:125], v[134:135]
	v_cvt_pk_bf16_f32 v124, v120, v121
	v_med3_f32 v120, v120, s68, v203
	v_med3_f32 v121, v121, s68, v203
	v_pk_fma_f32 v[116:117], v[116:117], v[126:127], v[136:137]
	v_pk_fma_f32 v[118:119], v[118:119], v[126:127], v[136:137]
	v_med3_f32 v126, v122, s68, v203
	v_cvt_pk_fp8_f32 v146, v120, v121
	v_med3_f32 v120, v123, s68, v203
	v_cvt_pk_fp8_f32 v147, v126, v120
	v_cvt_pk_bf16_f32 v125, v116, v117
	v_med3_f32 v116, v116, s68, v203
	v_med3_f32 v117, v117, s68, v203
	v_med3_f32 v121, v118, s68, v203
	v_cvt_pk_fp8_f32 v146, v116, v117 op_sel:[0,0,1]
	v_med3_f32 v116, v119, s68, v203
	v_cvt_pk_fp8_f32 v147, v121, v116 op_sel:[0,0,1]
	ds_write_b64 v187, v[124:125] offset:2560
	global_store_dword v[142:143], v146, off offset:1280
	v_cvt_pk_bf16_f32 v128, v122, v123
	v_cvt_pk_bf16_f32 v129, v118, v119
	global_store_dword v[166:167], v147, off offset:1280
	global_load_dwordx4 v[116:119], v[144:145], off offset:2048
	global_load_dwordx4 v[120:123], v[140:141], off offset:2048
	global_load_dwordx4 v[124:127], v[132:133], off offset:2048
	v_pk_mul_f32 v[130:131], v[174:175], v[178:179] op_sel_hi:[1,0]
	v_pk_mul_f32 v[134:135], v[176:177], v[168:169] op_sel_hi:[1,0]
	v_mov_b32_e32 v136, 0
	ds_write_b64 v158, v[128:129] offset:2560
	v_mov_b32_e32 v137, 0
	v_pk_mul_f32 v[128:129], v[172:173], v[168:169] op_sel_hi:[1,0]
	s_waitcnt vmcnt(2)
	v_pk_add_f32 v[116:117], v[116:117], 1.0 op_sel_hi:[1,0]
	v_pk_add_f32 v[118:119], v[118:119], 1.0 op_sel_hi:[1,0]
	s_waitcnt vmcnt(1)
	v_pk_mul_f32 v[116:117], v[120:121], v[116:117]
	v_pk_mul_f32 v[118:119], v[122:123], v[118:119]
	s_waitcnt vmcnt(0)
	v_pk_fma_f32 v[120:121], v[130:131], v[116:117], v[124:125]
	v_pk_fma_f32 v[70:71], v[70:71], v[118:119], v[126:127]
	v_pk_fma_f32 v[72:73], v[72:73], v[118:119], v[126:127]
	v_pk_fma_f32 v[116:117], v[134:135], v[116:117], v[124:125]
	v_cvt_pk_bf16_f32 v118, v120, v121
	v_med3_f32 v120, v120, s68, v203
	v_med3_f32 v121, v121, s68, v203
	v_med3_f32 v122, v116, s68, v203
	v_cvt_pk_fp8_f32 v136, v120, v121
	v_med3_f32 v120, v117, s68, v203
	v_cvt_pk_fp8_f32 v137, v122, v120
	v_cvt_pk_bf16_f32 v119, v70, v71
	v_med3_f32 v70, v70, s68, v203
	v_med3_f32 v71, v71, s68, v203
	v_med3_f32 v121, v72, s68, v203
	v_cvt_pk_fp8_f32 v136, v70, v71 op_sel:[0,0,1]
	v_med3_f32 v70, v73, s68, v203
	v_cvt_pk_fp8_f32 v137, v121, v70 op_sel:[0,0,1]
	ds_write_b64 v187, v[118:119] offset:3072
	global_store_dword v[142:143], v136, off offset:1536
	v_cvt_pk_bf16_f32 v124, v116, v117
	v_cvt_pk_bf16_f32 v125, v72, v73
	global_store_dword v[166:167], v137, off offset:1536
	global_load_dwordx4 v[70:73], v[144:145], off offset:3072
	global_load_dwordx4 v[116:119], v[140:141], off offset:3072
	global_load_dwordx4 v[120:123], v[132:133], off offset:3072
	v_pk_mul_f32 v[126:127], v[170:171], v[178:179] op_sel_hi:[1,0]
	v_mov_b32_e32 v130, 0
	ds_write_b64 v158, v[124:125] offset:3072
	v_mov_b32_e32 v131, 0
	s_waitcnt vmcnt(2)
	v_pk_add_f32 v[70:71], v[70:71], 1.0 op_sel_hi:[1,0]
	v_pk_add_f32 v[72:73], v[72:73], 1.0 op_sel_hi:[1,0]
	s_waitcnt vmcnt(1)
	v_pk_mul_f32 v[70:71], v[116:117], v[70:71]
	v_pk_mul_f32 v[72:73], v[118:119], v[72:73]
	s_waitcnt vmcnt(0)
	v_pk_fma_f32 v[116:117], v[126:127], v[70:71], v[120:121]
	v_pk_fma_f32 v[66:67], v[66:67], v[72:73], v[122:123]
	v_pk_fma_f32 v[68:69], v[68:69], v[72:73], v[122:123]
	v_pk_fma_f32 v[70:71], v[128:129], v[70:71], v[120:121]
	v_cvt_pk_bf16_f32 v72, v116, v117
	v_med3_f32 v116, v116, s68, v203
	v_med3_f32 v117, v117, s68, v203
	v_med3_f32 v118, v70, s68, v203
	v_cvt_pk_fp8_f32 v130, v116, v117
	v_med3_f32 v116, v71, s68, v203
	v_cvt_pk_fp8_f32 v131, v118, v116
	v_cvt_pk_bf16_f32 v73, v66, v67
	v_med3_f32 v66, v66, s68, v203
	v_med3_f32 v67, v67, s68, v203
	v_med3_f32 v117, v68, s68, v203
	v_cvt_pk_fp8_f32 v130, v66, v67 op_sel:[0,0,1]
	v_med3_f32 v66, v69, s68, v203
	v_cvt_pk_fp8_f32 v131, v117, v66 op_sel:[0,0,1]
	ds_write_b64 v187, v[72:73] offset:3584
	global_store_dword v[142:143], v130, off offset:1792
	v_cvt_pk_bf16_f32 v66, v70, v71
	v_cvt_pk_bf16_f32 v67, v68, v69
	global_store_dword v[166:167], v131, off offset:1792
	ds_write_b64 v158, v[66:67] offset:3584
	s_waitcnt lgkmcnt(0)
	s_barrier
.LBB0_1139:
	global_load_dword v240, v[92:93], off
	v_mov_b32_e32 v66, 0
	s_mov_b32 s16, 0
	v_mov_b64_e32 v[70:71], v[112:113]
	v_mov_b32_e32 v67, v66
	v_mov_b32_e32 v68, v66
	v_mov_b32_e32 v69, v66
.LBB0_1140:
	global_load_dwordx4 v[116:119], v[70:71], off offset:-256
	global_load_dwordx4 v[120:123], v[70:71], off offset:-192
	global_load_dwordx4 v[124:127], v[70:71], off offset:-128
	global_load_dwordx4 v[128:131], v[70:71], off offset:-64
	global_load_dwordx4 v[132:135], v[70:71], off
	global_load_dwordx4 v[136:139], v[70:71], off offset:64
	global_load_dwordx4 v[140:143], v[70:71], off offset:128
	global_load_dwordx4 v[144:147], v[70:71], off offset:192
	v_add_u32_e32 v72, s16, v1
	ds_read_b128 v[148:151], v72
	ds_read_b128 v[152:155], v72 offset:64
	s_addk_i32 s16, 0x200
	s_cmpk_eq_i32 s16, 0x800
	v_lshl_add_u64 v[70:71], v[70:71], 0, s[54:55]
	s_waitcnt vmcnt(7) lgkmcnt(1)
	v_mfma_f32_16x16x32_bf16 v[66:69], v[148:151], v[116:119], v[66:69]
	ds_read_b128 v[116:119], v72 offset:128
	s_waitcnt vmcnt(6) lgkmcnt(1)
	v_mfma_f32_16x16x32_bf16 v[66:69], v[152:155], v[120:123], v[66:69]
	ds_read_b128 v[120:123], v72 offset:192
	s_waitcnt vmcnt(5) lgkmcnt(1)
	v_mfma_f32_16x16x32_bf16 v[66:69], v[116:119], v[124:127], v[66:69]
	ds_read_b128 v[116:119], v72 offset:256
	s_waitcnt vmcnt(4) lgkmcnt(1)
	v_mfma_f32_16x16x32_bf16 v[66:69], v[120:123], v[128:131], v[66:69]
	ds_read_b128 v[120:123], v72 offset:320
	s_waitcnt vmcnt(3) lgkmcnt(1)
	v_mfma_f32_16x16x32_bf16 v[66:69], v[116:119], v[132:135], v[66:69]
	ds_read_b128 v[116:119], v72 offset:384
	s_waitcnt vmcnt(2) lgkmcnt(1)
	v_mfma_f32_16x16x32_bf16 v[66:69], v[120:123], v[136:139], v[66:69]
	ds_read_b128 v[120:123], v72 offset:448
	s_waitcnt vmcnt(1) lgkmcnt(1)
	v_mfma_f32_16x16x32_bf16 v[66:69], v[116:119], v[140:143], v[66:69]
	s_waitcnt vmcnt(0) lgkmcnt(0)
	v_mfma_f32_16x16x32_bf16 v[66:69], v[120:123], v[144:147], v[66:69]
	s_cbranch_scc0 .LBB0_1140
	s_nop 6
	ds_write2st64_b32 v200, v66, v67 offset1:1
	ds_write2st64_b32 v200, v68, v69 offset0:2 offset1:3
	s_nop 1
	s_and_b64 vcc, exec, s[56:57]
	s_cbranch_vccnz .Lp7_nopf
	s_add_i32 s16, s73, s62
	s_ashr_i32 s17, s16, 31
	s_or_b32 s18, s16, 1
	s_lshl_b64 s[20:21], s[16:17], 13
	v_readlane_b32 s76, v252, 9
	v_readlane_b32 s77, v252, 10
	s_add_u32 s20, s76, s20
	s_addc_u32 s21, s77, s21
	s_ashr_i32 s19, s18, 31
	s_lshl_b64 s[22:23], s[18:19], 13
	s_add_u32 s22, s76, s22
	s_addc_u32 s23, s77, s23
	s_lshl_b64 s[16:17], s[16:17], 12
	v_lshl_add_u64 v[66:67], v[100:101], 0, s[16:17]
	s_lshl_b64 s[16:17], s[18:19], 12
	v_lshl_add_u64 v[68:69], v[100:101], 0, s[16:17]
	global_load_dwordx4 v[2:5], v195, s[20:21]
	global_load_dwordx4 v[6:9], v195, s[20:21] offset:1024
	global_load_dwordx4 v[10:13], v195, s[22:23]
	global_load_dwordx4 v[14:17], v195, s[22:23] offset:1024
	global_load_dwordx4 v[18:21], v195, s[20:21] offset:2048
	global_load_dwordx4 v[22:25], v195, s[20:21] offset:3072
	global_load_dwordx4 v[26:29], v195, s[22:23] offset:2048
	global_load_dwordx4 v[30:33], v195, s[22:23] offset:3072
	global_load_dwordx2 v[74:75], v[66:67], off
	global_load_dwordx2 v[76:77], v[66:67], off offset:512
	global_load_dwordx2 v[78:79], v[66:67], off offset:1024
	global_load_dwordx2 v[80:81], v[66:67], off offset:1536
	global_load_dwordx2 v[82:83], v[68:69], off
	global_load_dwordx2 v[84:85], v[68:69], off offset:512
	global_load_dwordx2 v[88:89], v[68:69], off offset:1024
	global_load_dwordx2 v[90:91], v[68:69], off offset:1536
	global_load_dwordx4 v[34:37], v196, s[20:21]
	global_load_dwordx4 v[38:41], v196, s[22:23]
	global_load_dwordx4 v[42:45], v197, s[20:21]
	global_load_dwordx4 v[46:49], v197, s[22:23]
	global_load_dwordx4 v[50:53], v198, s[20:21]
	global_load_dwordx4 v[54:57], v198, s[22:23]
	global_load_dwordx4 v[58:61], v199, s[20:21]
	global_load_dwordx4 v[62:65], v199, s[22:23]
	global_load_dwordx2 v[94:95], v[66:67], off offset:2048
	global_load_dwordx2 v[96:97], v[66:67], off offset:2560
	global_load_dwordx2 v[98:99], v[66:67], off offset:3072
	global_load_dwordx2 v[102:103], v[66:67], off offset:3584
	global_load_dwordx2 v[104:105], v[68:69], off offset:2048
	global_load_dwordx2 v[106:107], v[68:69], off offset:2560
	global_load_dwordx2 v[108:109], v[68:69], off offset:3072
	global_load_dwordx2 v[110:111], v[68:69], off offset:3584
	v_readlane_b32 s78, v252, 11
	v_readlane_b32 s79, v252, 12
	v_readlane_b32 s80, v252, 13
	v_readlane_b32 s81, v252, 14
	v_readlane_b32 s82, v252, 15
	v_readlane_b32 s83, v252, 16
	v_readlane_b32 s84, v252, 17
	v_readlane_b32 s85, v252, 18
	v_readlane_b32 s86, v252, 19
	v_readlane_b32 s87, v252, 20
	v_readlane_b32 s88, v252, 21
	v_readlane_b32 s89, v252, 22
	v_readlane_b32 s90, v252, 23
	v_readlane_b32 s91, v252, 24
.Lp7_nopf:
	s_waitcnt lgkmcnt(0)
	s_barrier
	s_mov_b32 s16, 0
	s_mov_b64 s[58:59], -1
	s_branch .LBB0_1143

.LBB0_1143:
	s_mov_b32 s98, 0xffff0000
	s_mov_b32 s99, 0xffff0000
	s_mov_b32 s100, 0
	s_mov_b32 s101, -1
	s_or_b32 s74, s16, s62
	v_lshl_add_u32 v66, s74, 8, v194
	ds_read2st64_b32 v[66:67], v66 offset1:16
	s_waitcnt lgkmcnt(0)
	v_add_f32_e32 v66, v66, v67
	v_mul_f32_e32 v67, 0xbfb8aa3b, v66
	v_fma_f32 v68, v66, s70, -v67
	v_rndne_f32_e32 v69, v67
	v_fmac_f32_e32 v68, 0xb2a5705f, v66
	v_sub_f32_e32 v67, v67, v69
	v_add_f32_e32 v67, v67, v68
	v_exp_f32_e32 v67, v67
	v_cvt_i32_f32_e32 v68, v69
	v_cmp_nlt_f32_e32 vcc, s71, v66
	v_ldexp_f32 v67, v67, v68
	s_nop 0
	v_cndmask_b32_e32 v67, 0, v67, vcc
	v_cmp_ngt_f32_e32 vcc, s72, v66
	s_nop 1
	v_cndmask_b32_e32 v66, v204, v67, vcc
	v_add_f32_e32 v66, 1.0, v66
	v_div_scale_f32 v67, s[16:17], v66, v66, 1.0
	v_rcp_f32_e32 v68, v67
	s_nop 0
	v_fma_f32 v69, -v67, v68, 1.0
	v_fmac_f32_e32 v68, v69, v68
	v_div_scale_f32 v69, vcc, 1.0, v66, 1.0
	v_mul_f32_e32 v70, v69, v68
	v_fma_f32 v71, -v67, v70, v69
	v_fmac_f32_e32 v70, v71, v68
	v_fma_f32 v67, -v67, v70, v69
	v_div_fmas_f32 v67, v67, v68, v70
	v_div_fixup_f32 v66, v67, v66, 1.0
	v_mov_b32_e32 v67, v240
	v_add_f32_e32 v67, v67, v66
	s_nop 1
	v_mov_b32_dpp v68, v67 quad_perm:[1,0,3,2] row_mask:0xf bank_mask:0xf
	s_waitcnt lgkmcnt(0)
	v_max_f32_e32 v68, v68, v68
	v_max_f32_e32 v68, v67, v68
	s_nop 1
	v_mov_b32_dpp v69, v68 quad_perm:[2,3,0,1] row_mask:0xf bank_mask:0xf
	s_waitcnt lgkmcnt(0)
	v_max_f32_e32 v69, v69, v69
	v_max_f32_e32 v68, v68, v69
	s_nop 1
	v_mov_b32_dpp v69, v68 row_shl:4 row_mask:0xf bank_mask:0x5
	v_mov_b32_dpp v69, v68 row_shr:4 row_mask:0xf bank_mask:0xa
	s_waitcnt lgkmcnt(0)
	v_max_f32_e32 v69, v69, v69
	v_max_f32_e32 v70, v68, v69
	v_cmp_eq_f32_e32 vcc, v67, v70
	s_nop 1
	v_and_b32_e32 v69, vcc_hi, v87
	v_and_b32_e32 v68, vcc_lo, v86
	v_cmp_ne_u64_e32 vcc, 0, v[68:69]
	v_ffbl_b32_e32 v69, v69
	v_add_u32_e32 v69, 32, v69
	v_ffbl_b32_e32 v68, v68
	v_min_u32_e32 v68, v68, v69
	v_cmp_eq_u32_e64 s[16:17], v206, v68
	s_and_b64 vcc, vcc, s[16:17]
	v_cndmask_b32_e32 v68, v67, v205, vcc
	s_nop 1
	v_mov_b32_dpp v69, v68 quad_perm:[1,0,3,2] row_mask:0xf bank_mask:0xf
	s_waitcnt lgkmcnt(0)
	v_max_f32_e32 v69, v69, v69
	v_max_f32_e32 v68, v68, v69
	s_nop 1
	v_mov_b32_dpp v69, v68 quad_perm:[2,3,0,1] row_mask:0xf bank_mask:0xf
	s_waitcnt lgkmcnt(0)
	v_max_f32_e32 v69, v69, v69
	v_max_f32_e32 v68, v68, v69
	s_nop 1
	v_mov_b32_dpp v69, v68 row_shl:4 row_mask:0xf bank_mask:0x5
	v_mov_b32_dpp v69, v68 row_shr:4 row_mask:0xf bank_mask:0xa
	s_waitcnt lgkmcnt(0)
	v_max_f32_e32 v69, v69, v69
	v_max_f32_e32 v68, v68, v69
	v_add_f32_e32 v68, v70, v68
	s_nop 0
	v_readlane_b32 s16, v68, 0
	s_nop 1
	v_cmp_gt_f32_e32 vcc, s16, v68
	v_cmp_eq_f32_e64 s[16:17], s16, v68
	s_and_b64 s[16:17], s[2:3], s[16:17]
	s_or_b64 s[16:17], vcc, s[16:17]
	v_cndmask_b32_e64 v69, 0, 1, s[16:17]
	v_readlane_b32 s16, v68, 8
	s_nop 1
	v_cmp_gt_f32_e32 vcc, s16, v68
	v_cmp_eq_f32_e64 s[16:17], s16, v68
	s_and_b64 s[16:17], s[4:5], s[16:17]
	s_or_b64 s[16:17], vcc, s[16:17]
	v_cndmask_b32_e64 v70, 0, 1, s[16:17]
	v_readlane_b32 s16, v68, 16
	s_nop 1
	v_cmp_gt_f32_e32 vcc, s16, v68
	v_cmp_eq_f32_e64 s[16:17], s16, v68
	s_and_b64 s[16:17], s[6:7], s[16:17]
	s_or_b64 s[16:17], vcc, s[16:17]
	v_cndmask_b32_e64 v71, 0, 1, s[16:17]
	v_readlane_b32 s16, v68, 24
	v_add3_u32 v69, v69, v70, v71
	s_nop 0
	v_cmp_gt_f32_e32 vcc, s16, v68
	v_cmp_eq_f32_e64 s[16:17], s16, v68
	s_and_b64 s[16:17], s[8:9], s[16:17]
	s_or_b64 s[16:17], vcc, s[16:17]
	v_cndmask_b32_e64 v70, 0, 1, s[16:17]
	v_readlane_b32 s16, v68, 32
	s_nop 1
	v_cmp_gt_f32_e32 vcc, s16, v68
	v_cmp_eq_f32_e64 s[16:17], s16, v68
	s_and_b64 s[16:17], s[10:11], s[16:17]
	s_or_b64 s[16:17], vcc, s[16:17]
	v_cndmask_b32_e64 v71, 0, 1, s[16:17]
	v_readlane_b32 s16, v68, 40
	v_add3_u32 v69, v69, v70, v71
	s_nop 0
	v_cmp_gt_f32_e32 vcc, s16, v68
	v_cmp_eq_f32_e64 s[16:17], s16, v68
	s_and_b64 s[16:17], s[12:13], s[16:17]
	s_or_b64 s[16:17], vcc, s[16:17]
	v_cndmask_b32_e64 v70, 0, 1, s[16:17]
	v_readlane_b32 s16, v68, 48
	s_nop 1
	v_cmp_gt_f32_e32 vcc, s16, v68
	v_cmp_eq_f32_e64 s[16:17], s16, v68
	s_and_b64 s[16:17], s[14:15], s[16:17]
	s_or_b64 s[16:17], vcc, s[16:17]
	v_cndmask_b32_e64 v71, 0, 1, s[16:17]
	v_readlane_b32 s16, v68, 56
	s_nop 1
	v_cmp_gt_f32_e32 vcc, s16, v68
	s_nop 1
	v_addc_co_u32_e32 v68, vcc, v69, v70, vcc
	v_add_u32_e32 v68, v68, v71
	v_cmp_gt_u32_e32 vcc, 4, v68
	s_nop 1
	v_cndmask_b32_e32 v67, v205, v67, vcc
	s_nop 1
	v_mov_b32_dpp v68, v67 quad_perm:[1,0,3,2] row_mask:0xf bank_mask:0xf
	s_waitcnt lgkmcnt(0)
	v_max_f32_e32 v68, v68, v68
	v_max_f32_e32 v68, v67, v68
	s_nop 1
	v_mov_b32_dpp v69, v68 quad_perm:[2,3,0,1] row_mask:0xf bank_mask:0xf
	s_waitcnt lgkmcnt(0)
	v_max_f32_e32 v69, v69, v69
	v_max_f32_e32 v68, v68, v69
	s_nop 1
	v_mov_b32_dpp v69, v68 row_shl:4 row_mask:0xf bank_mask:0x5
	v_mov_b32_dpp v69, v68 row_shr:4 row_mask:0xf bank_mask:0xa
	s_waitcnt lgkmcnt(0)
	v_max_f32_e32 v69, v69, v69
	v_max_f32_e32 v68, v68, v69
	s_nop 1
	v_mov_b32_dpp v69, v68 row_ror:8 row_mask:0xf bank_mask:0xf
	s_waitcnt lgkmcnt(0)
	v_max_f32_e32 v69, v69, v69
	v_max_f32_e32 v68, v68, v69
	v_mov_b32_e32 v69, v68
	v_mov_b32_e32 v239, v68
	s_nop 1
	v_permlane16_swap_b32_e32 v69, v239
	v_cndmask_b32_e64 v69, v239, v69, s[98:99]
	s_waitcnt lgkmcnt(0)
	v_max_f32_e32 v69, v69, v69
	v_max_f32_e32 v68, v68, v69
	v_mov_b32_e32 v69, v68
	v_mov_b32_e32 v239, v68
	s_nop 1
	v_permlane32_swap_b32_e32 v69, v239
	v_cndmask_b32_e64 v69, v239, v69, s[100:101]
	s_waitcnt lgkmcnt(0)
	v_max_f32_e32 v69, v69, v69
	v_max_f32_e32 v68, v68, v69
	v_cmp_eq_f32_e32 vcc, v67, v68
	s_cmp_lg_u64 vcc, 0
	s_ff1_i32_b64 s18, vcc
	s_cselect_b64 s[16:17], -1, 0
	v_cmp_eq_u32_e32 vcc, s18, v206
	s_and_b64 vcc, s[16:17], vcc
	s_nop 0
	v_cndmask_b32_e32 v67, v67, v205, vcc
	s_nop 1
	v_mov_b32_dpp v68, v67 quad_perm:[1,0,3,2] row_mask:0xf bank_mask:0xf
	s_waitcnt lgkmcnt(0)
	v_max_f32_e32 v68, v68, v68
	v_max_f32_e32 v68, v67, v68
	s_nop 1
	v_mov_b32_dpp v69, v68 quad_perm:[2,3,0,1] row_mask:0xf bank_mask:0xf
	s_waitcnt lgkmcnt(0)
	v_max_f32_e32 v69, v69, v69
	v_max_f32_e32 v68, v68, v69
	s_nop 1
	v_mov_b32_dpp v69, v68 row_shl:4 row_mask:0xf bank_mask:0x5
	v_mov_b32_dpp v69, v68 row_shr:4 row_mask:0xf bank_mask:0xa
	s_waitcnt lgkmcnt(0)
	v_max_f32_e32 v69, v69, v69
	v_max_f32_e32 v68, v68, v69
	s_nop 1
	v_mov_b32_dpp v69, v68 row_ror:8 row_mask:0xf bank_mask:0xf
	s_waitcnt lgkmcnt(0)
	v_max_f32_e32 v69, v69, v69
	v_max_f32_e32 v68, v68, v69
	v_mov_b32_e32 v69, v68
	v_mov_b32_e32 v239, v68
	s_nop 1
	v_permlane16_swap_b32_e32 v69, v239
	v_cndmask_b32_e64 v69, v239, v69, s[98:99]
	s_waitcnt lgkmcnt(0)
	v_max_f32_e32 v69, v69, v69
	v_max_f32_e32 v68, v68, v69
	v_mov_b32_e32 v69, v68
	v_mov_b32_e32 v239, v68
	s_nop 1
	v_permlane32_swap_b32_e32 v69, v239
	v_cndmask_b32_e64 v69, v239, v69, s[100:101]
	s_waitcnt lgkmcnt(0)
	v_max_f32_e32 v69, v69, v69
	v_max_f32_e32 v68, v68, v69
	v_cmp_eq_f32_e64 s[16:17], v67, v68
	s_cmp_lg_u64 s[16:17], 0
	s_ff1_i32_b64 s16, s[16:17]
	s_cselect_b64 s[18:19], -1, 0
	v_cmp_eq_u32_e64 s[16:17], s16, v206
	s_and_b64 s[16:17], s[18:19], s[16:17]
	s_nop 0
	v_cndmask_b32_e64 v67, v67, v205, s[16:17]
	s_nop 1
	v_mov_b32_dpp v68, v67 quad_perm:[1,0,3,2] row_mask:0xf bank_mask:0xf
	s_waitcnt lgkmcnt(0)
	v_max_f32_e32 v68, v68, v68
	v_max_f32_e32 v68, v67, v68
	s_nop 1
	v_mov_b32_dpp v69, v68 quad_perm:[2,3,0,1] row_mask:0xf bank_mask:0xf
	s_waitcnt lgkmcnt(0)
	v_max_f32_e32 v69, v69, v69
	v_max_f32_e32 v68, v68, v69
	s_nop 1
	v_mov_b32_dpp v69, v68 row_shl:4 row_mask:0xf bank_mask:0x5
	v_mov_b32_dpp v69, v68 row_shr:4 row_mask:0xf bank_mask:0xa
	s_waitcnt lgkmcnt(0)
	v_max_f32_e32 v69, v69, v69
	v_max_f32_e32 v68, v68, v69
	s_nop 1
	v_mov_b32_dpp v69, v68 row_ror:8 row_mask:0xf bank_mask:0xf
	s_waitcnt lgkmcnt(0)
	v_max_f32_e32 v69, v69, v69
	v_max_f32_e32 v68, v68, v69
	v_mov_b32_e32 v69, v68
	v_mov_b32_e32 v239, v68
	s_nop 1
	v_permlane16_swap_b32_e32 v69, v239
	v_cndmask_b32_e64 v69, v239, v69, s[98:99]
	s_waitcnt lgkmcnt(0)
	v_max_f32_e32 v69, v69, v69
	v_max_f32_e32 v68, v68, v69
	v_mov_b32_e32 v69, v68
	v_mov_b32_e32 v239, v68
	s_nop 1
	v_permlane32_swap_b32_e32 v69, v239
	v_cndmask_b32_e64 v69, v239, v69, s[100:101]
	s_waitcnt lgkmcnt(0)
	v_max_f32_e32 v69, v69, v69
	v_max_f32_e32 v68, v68, v69
	v_cmp_eq_f32_e64 s[18:19], v67, v68
	s_cmp_lg_u64 s[18:19], 0
	s_ff1_i32_b64 s18, s[18:19]
	s_cselect_b64 s[20:21], -1, 0
	v_cmp_eq_u32_e64 s[18:19], s18, v206
	s_and_b64 s[18:19], s[20:21], s[18:19]
	s_nop 0
	v_cndmask_b32_e64 v67, v67, v205, s[18:19]
	s_nop 1
	v_mov_b32_dpp v68, v67 quad_perm:[1,0,3,2] row_mask:0xf bank_mask:0xf
	s_waitcnt lgkmcnt(0)
	v_max_f32_e32 v68, v68, v68
	v_max_f32_e32 v68, v67, v68
	s_nop 1
	v_mov_b32_dpp v69, v68 quad_perm:[2,3,0,1] row_mask:0xf bank_mask:0xf
	s_waitcnt lgkmcnt(0)
	v_max_f32_e32 v69, v69, v69
	v_max_f32_e32 v68, v68, v69
	s_nop 1
	v_mov_b32_dpp v69, v68 row_shl:4 row_mask:0xf bank_mask:0x5
	v_mov_b32_dpp v69, v68 row_shr:4 row_mask:0xf bank_mask:0xa
	s_waitcnt lgkmcnt(0)
	v_max_f32_e32 v69, v69, v69
	v_max_f32_e32 v68, v68, v69
	s_nop 1
	v_mov_b32_dpp v69, v68 row_ror:8 row_mask:0xf bank_mask:0xf
	s_waitcnt lgkmcnt(0)
	v_max_f32_e32 v69, v69, v69
	v_max_f32_e32 v68, v68, v69
	v_mov_b32_e32 v69, v68
	v_mov_b32_e32 v239, v68
	s_nop 1
	v_permlane16_swap_b32_e32 v69, v239
	v_cndmask_b32_e64 v69, v239, v69, s[98:99]
	s_waitcnt lgkmcnt(0)
	v_max_f32_e32 v69, v69, v69
	v_max_f32_e32 v68, v68, v69
	v_mov_b32_e32 v69, v68
	v_mov_b32_e32 v239, v68
	s_nop 1
	v_permlane32_swap_b32_e32 v69, v239
	v_cndmask_b32_e64 v69, v239, v69, s[100:101]
	s_waitcnt lgkmcnt(0)
	v_max_f32_e32 v69, v69, v69
	v_max_f32_e32 v68, v68, v69
	v_cmp_eq_f32_e64 s[20:21], v67, v68
	s_cmp_lg_u64 s[20:21], 0
	s_ff1_i32_b64 s20, s[20:21]
	s_cselect_b64 s[22:23], -1, 0
	v_cmp_eq_u32_e64 s[20:21], s20, v206
	s_and_b64 s[20:21], s[22:23], s[20:21]
	s_nop 0
	v_cndmask_b32_e64 v67, v67, v205, s[20:21]
	s_nop 1
	v_mov_b32_dpp v68, v67 quad_perm:[1,0,3,2] row_mask:0xf bank_mask:0xf
	s_waitcnt lgkmcnt(0)
	v_max_f32_e32 v68, v68, v68
	v_max_f32_e32 v68, v67, v68
	s_nop 1
	v_mov_b32_dpp v69, v68 quad_perm:[2,3,0,1] row_mask:0xf bank_mask:0xf
	s_waitcnt lgkmcnt(0)
	v_max_f32_e32 v69, v69, v69
	v_max_f32_e32 v68, v68, v69
	s_nop 1
	v_mov_b32_dpp v69, v68 row_shl:4 row_mask:0xf bank_mask:0x5
	v_mov_b32_dpp v69, v68 row_shr:4 row_mask:0xf bank_mask:0xa
	s_waitcnt lgkmcnt(0)
	v_max_f32_e32 v69, v69, v69
	v_max_f32_e32 v68, v68, v69
	s_nop 1
	v_mov_b32_dpp v69, v68 row_ror:8 row_mask:0xf bank_mask:0xf
	s_waitcnt lgkmcnt(0)
	v_max_f32_e32 v69, v69, v69
	v_max_f32_e32 v68, v68, v69
	v_mov_b32_e32 v69, v68
	v_mov_b32_e32 v239, v68
	s_nop 1
	v_permlane16_swap_b32_e32 v69, v239
	v_cndmask_b32_e64 v69, v239, v69, s[98:99]
	s_waitcnt lgkmcnt(0)
	v_max_f32_e32 v69, v69, v69
	v_max_f32_e32 v68, v68, v69
	v_mov_b32_e32 v69, v68
	v_mov_b32_e32 v239, v68
	s_nop 1
	v_permlane32_swap_b32_e32 v69, v239
	v_cndmask_b32_e64 v69, v239, v69, s[100:101]
	s_waitcnt lgkmcnt(0)
	v_max_f32_e32 v69, v69, v69
	v_max_f32_e32 v68, v68, v69
	v_cmp_eq_f32_e64 s[22:23], v67, v68
	s_cmp_lg_u64 s[22:23], 0
	s_ff1_i32_b64 s22, s[22:23]
	s_cselect_b64 s[24:25], -1, 0
	v_cmp_eq_u32_e64 s[22:23], s22, v206
	s_and_b64 s[22:23], s[24:25], s[22:23]
	s_nop 0
	v_cndmask_b32_e64 v67, v67, v205, s[22:23]
	s_nop 1
	v_mov_b32_dpp v68, v67 quad_perm:[1,0,3,2] row_mask:0xf bank_mask:0xf
	v_max_f32_e32 v69, v67, v67
	s_waitcnt lgkmcnt(0)
	v_max_f32_e32 v68, v68, v68
	v_max_f32_e32 v68, v69, v68
	s_nop 1
	v_mov_b32_dpp v69, v68 quad_perm:[2,3,0,1] row_mask:0xf bank_mask:0xf
	s_waitcnt lgkmcnt(0)
	v_max_f32_e32 v69, v69, v69
	v_max_f32_e32 v68, v68, v69
	s_nop 1
	v_mov_b32_dpp v69, v68 row_shl:4 row_mask:0xf bank_mask:0x5
	v_mov_b32_dpp v69, v68 row_shr:4 row_mask:0xf bank_mask:0xa
	s_waitcnt lgkmcnt(0)
	v_max_f32_e32 v69, v69, v69
	v_max_f32_e32 v68, v68, v69
	s_nop 1
	v_mov_b32_dpp v69, v68 row_ror:8 row_mask:0xf bank_mask:0xf
	s_waitcnt lgkmcnt(0)
	v_max_f32_e32 v69, v69, v69
	v_max_f32_e32 v68, v68, v69
	v_mov_b32_e32 v69, v68
	v_mov_b32_e32 v239, v68
	s_nop 1
	v_permlane16_swap_b32_e32 v69, v239
	v_cndmask_b32_e64 v69, v239, v69, s[98:99]
	s_waitcnt lgkmcnt(0)
	v_max_f32_e32 v69, v69, v69
	v_max_f32_e32 v68, v68, v69
	v_mov_b32_e32 v69, v68
	v_mov_b32_e32 v239, v68
	s_nop 1
	v_permlane32_swap_b32_e32 v69, v239
	v_cndmask_b32_e64 v69, v239, v69, s[100:101]
	s_waitcnt lgkmcnt(0)
	v_max_f32_e32 v69, v69, v69
	v_max_f32_e32 v68, v68, v69
	v_cmp_eq_f32_e64 s[24:25], v67, v68
	s_cmp_lg_u64 s[24:25], 0
	s_ff1_i32_b64 s24, s[24:25]
	s_cselect_b64 s[26:27], -1, 0
	v_cmp_eq_u32_e64 s[24:25], s24, v206
	s_and_b64 s[24:25], s[26:27], s[24:25]
	s_nop 0
	v_cndmask_b32_e64 v67, v67, v205, s[24:25]
	s_nop 1
	v_mov_b32_dpp v68, v67 quad_perm:[1,0,3,2] row_mask:0xf bank_mask:0xf
	v_max_f32_e32 v69, v67, v67
	s_waitcnt lgkmcnt(0)
	v_max_f32_e32 v68, v68, v68
	v_max_f32_e32 v68, v69, v68
	s_nop 1
	v_mov_b32_dpp v69, v68 quad_perm:[2,3,0,1] row_mask:0xf bank_mask:0xf
	s_waitcnt lgkmcnt(0)
	v_max_f32_e32 v69, v69, v69
	v_max_f32_e32 v68, v68, v69
	s_nop 1
	v_mov_b32_dpp v69, v68 row_shl:4 row_mask:0xf bank_mask:0x5
	v_mov_b32_dpp v69, v68 row_shr:4 row_mask:0xf bank_mask:0xa
	s_waitcnt lgkmcnt(0)
	v_max_f32_e32 v69, v69, v69
	v_max_f32_e32 v68, v68, v69
	s_nop 1
	v_mov_b32_dpp v69, v68 row_ror:8 row_mask:0xf bank_mask:0xf
	s_waitcnt lgkmcnt(0)
	v_max_f32_e32 v69, v69, v69
	v_max_f32_e32 v68, v68, v69
	v_mov_b32_e32 v69, v68
	v_mov_b32_e32 v239, v68
	s_nop 1
	v_permlane16_swap_b32_e32 v69, v239
	v_cndmask_b32_e64 v69, v239, v69, s[98:99]
	s_waitcnt lgkmcnt(0)
	v_max_f32_e32 v69, v69, v69
	v_max_f32_e32 v68, v68, v69
	v_mov_b32_e32 v69, v68
	v_mov_b32_e32 v239, v68
	s_nop 1
	v_permlane32_swap_b32_e32 v69, v239
	v_cndmask_b32_e64 v69, v239, v69, s[100:101]
	s_waitcnt lgkmcnt(0)
	v_max_f32_e32 v69, v69, v69
	v_max_f32_e32 v68, v68, v69
	v_cmp_eq_f32_e64 s[26:27], v67, v68
	s_cmp_lg_u64 s[26:27], 0
	s_ff1_i32_b64 s26, s[26:27]
	s_cselect_b64 s[28:29], -1, 0
	v_cmp_eq_u32_e64 s[26:27], s26, v206
	s_and_b64 s[26:27], s[28:29], s[26:27]
	s_nop 0
	v_cndmask_b32_e64 v67, v67, v205, s[26:27]
	s_nop 1
	v_mov_b32_dpp v68, v67 quad_perm:[1,0,3,2] row_mask:0xf bank_mask:0xf
	v_max_f32_e32 v69, v67, v67
	s_waitcnt lgkmcnt(0)
	v_max_f32_e32 v68, v68, v68
	v_max_f32_e32 v68, v69, v68
	s_nop 1
	v_mov_b32_dpp v69, v68 quad_perm:[2,3,0,1] row_mask:0xf bank_mask:0xf
	s_waitcnt lgkmcnt(0)
	v_max_f32_e32 v69, v69, v69
	v_max_f32_e32 v68, v68, v69
	s_nop 1
	v_mov_b32_dpp v69, v68 row_shl:4 row_mask:0xf bank_mask:0x5
	v_mov_b32_dpp v69, v68 row_shr:4 row_mask:0xf bank_mask:0xa
	s_waitcnt lgkmcnt(0)
	v_max_f32_e32 v69, v69, v69
	v_max_f32_e32 v68, v68, v69
	s_nop 1
	v_mov_b32_dpp v69, v68 row_ror:8 row_mask:0xf bank_mask:0xf
	s_waitcnt lgkmcnt(0)
	v_max_f32_e32 v69, v69, v69
	v_max_f32_e32 v68, v68, v69
	v_mov_b32_e32 v69, v68
	v_mov_b32_e32 v239, v68
	s_nop 1
	v_permlane16_swap_b32_e32 v69, v239
	v_cndmask_b32_e64 v69, v239, v69, s[98:99]
	s_waitcnt lgkmcnt(0)
	v_max_f32_e32 v69, v69, v69
	v_max_f32_e32 v68, v68, v69
	v_mov_b32_e32 v69, v68
	v_mov_b32_e32 v239, v68
	s_nop 1
	v_permlane32_swap_b32_e32 v69, v239
	v_cndmask_b32_e64 v69, v239, v69, s[100:101]
	s_waitcnt lgkmcnt(0)
	v_max_f32_e32 v69, v69, v69
	v_max_f32_e32 v68, v68, v69
	v_cmp_eq_f32_e64 s[28:29], v67, v68
	s_cmp_lg_u64 s[28:29], 0
	s_ff1_i32_b64 s28, s[28:29]
	s_cselect_b64 s[76:77], -1, 0
	v_cmp_eq_u32_e64 s[28:29], s28, v206
	s_and_b64 s[28:29], s[76:77], s[28:29]
	s_or_b64 s[26:27], s[28:29], s[26:27]
	s_or_b64 s[24:25], s[26:27], s[24:25]
	s_or_b64 s[22:23], s[24:25], s[22:23]
	s_or_b64 s[20:21], s[22:23], s[20:21]
	s_or_b64 s[18:19], s[20:21], s[18:19]
	s_or_b64 s[16:17], s[18:19], s[16:17]
	s_or_b64 s[16:17], s[16:17], vcc
	v_cndmask_b32_e64 v67, 0, v66, s[16:17]
	s_nop 1
	v_mov_b32_dpp v68, v67 quad_perm:[1,0,3,2] row_mask:0xf bank_mask:0xf
	v_cndmask_b32_e64 v69, 0, 1, s[16:17]
	v_cmp_ne_u32_e32 vcc, 0, v69
	s_waitcnt lgkmcnt(0)
	v_add_f32_e32 v67, v67, v68
	s_nop 1
	v_mov_b32_dpp v68, v67 quad_perm:[2,3,0,1] row_mask:0xf bank_mask:0xf
	s_waitcnt lgkmcnt(0)
	v_add_f32_e32 v67, v67, v68
	s_nop 1
	v_mov_b32_dpp v68, v67 row_shl:4 row_mask:0xf bank_mask:0x5
	v_mov_b32_dpp v68, v67 row_shr:4 row_mask:0xf bank_mask:0xa
	s_waitcnt lgkmcnt(0)
	v_add_f32_e32 v67, v67, v68
	s_nop 1
	v_mov_b32_dpp v68, v67 row_ror:8 row_mask:0xf bank_mask:0xf
	s_waitcnt lgkmcnt(0)
	v_add_f32_e32 v67, v67, v68
	v_mov_b32_e32 v68, v67
	v_mov_b32_e32 v239, v67
	s_nop 1
	v_permlane16_swap_b32_e32 v68, v239
	v_cndmask_b32_e64 v68, v239, v68, s[98:99]
	s_waitcnt lgkmcnt(0)
	v_add_f32_e32 v67, v67, v68
	v_mov_b32_e32 v68, v67
	v_mov_b32_e32 v239, v67
	s_nop 1
	v_permlane32_swap_b32_e32 v68, v239
	v_cndmask_b32_e64 v68, v239, v68, s[100:101]
	s_and_saveexec_b64 s[18:19], s[16:17]
	s_cbranch_execz .LBB0_1142
	s_add_i32 s74, s74, s63
	s_cmpk_gt_i32 s74, 0x3fff
	s_waitcnt lgkmcnt(0)
	v_add_f32_e32 v67, v67, v68
	v_mbcnt_lo_u32_b32 v68, vcc_lo, 0
	s_cselect_b32 s16, 0x100, 0
	v_mbcnt_hi_u32_b32 v68, vcc_hi, v68
	v_add_u32_e32 v69, s16, v115
	ds_add_rtn_u32 v72, v69, v201
	v_lshl_add_u32 v68, s74, 3, v68
	v_div_scale_f32 v73, s[16:17], v67, v67, v66
	v_ashrrev_i32_e32 v69, 31, v68
	v_rcp_f32_e32 v116, v73
	v_lshlrev_b64 v[68:69], 2, v[68:69]
	v_lshl_add_u64 v[70:71], s[36:37], 0, v[68:69]
	global_store_dword v[70:71], v206, off
	v_lshl_add_u64 v[70:71], s[38:39], 0, v[68:69]
	s_waitcnt lgkmcnt(0)
	global_store_dword v[70:71], v72, off
	v_fma_f32 v70, -v73, v116, 1.0
	v_fmac_f32_e32 v116, v70, v116
	v_div_scale_f32 v70, vcc, v66, v67, v66
	v_mul_f32_e32 v71, v70, v116
	v_fma_f32 v72, -v73, v71, v70
	v_fmac_f32_e32 v71, v72, v116
	v_fma_f32 v70, -v73, v71, v70
	v_div_fmas_f32 v70, v70, v116, v71
	v_div_fixup_f32 v66, v70, v67, v66
	v_mul_f32_e32 v70, 0x40200000, v66
	v_lshl_add_u64 v[66:67], s[40:41], 0, v[68:69]
	global_store_dword v[66:67], v70, off
	s_branch .LBB0_1142
